# speedup vs baseline: 1.0438x; 1.0215x over previous
.Lk2f_w7b:
	v_sub_u32_e32 v16, v12, v4
	v_sub_u32_e32 v17, v13, v4
	v_add_u32_e32 v20, v17, v15
	v_readfirstlane_b32 s39, v4
	v_readlane_b32 s38, v20, 63
	s_lshl_b32 s39, s39, 2
	s_cmpk_gt_u32 s38, 0x480
	s_cbranch_scc1 .Lk2f_w7slow
	v_min_u32_e32 v18, 48, v1
	v_mul_u32_u24_e32 v18, 0x120, v18
	v_lshlrev_b32_e32 v16, 2, v16
	v_lshlrev_b32_e32 v17, 2, v17
	v_max_i32_e32 v19, v14, v15
	s_mov_b32 s5, 0
.Lk2f_w7c:
	v_cmp_lt_i32_e32 vcc, s5, v19
	s_cmp_lg_u64 vcc, 0
	s_cbranch_scc0 .Lk2f_w7w
	ds_read_b128 v[20:23], v18 offset:19456
	ds_read_b128 v[24:27], v18 offset:19600
	v_subrev_u32_e32 v28, s5, v14
	v_subrev_u32_e32 v29, s5, v15
	s_waitcnt lgkmcnt(0)
	v_cmp_lt_i32_e32 vcc, 0, v28
	s_and_saveexec_b64 s[40:41], vcc
	s_cbranch_execz .Lk2f_w7d0
	ds_write_b32 v16, v20 offset:33712
.Lk2f_w7d0:
	s_mov_b64 exec, s[40:41]
	v_cmp_lt_i32_e32 vcc, 1, v28
	s_and_saveexec_b64 s[40:41], vcc
	s_cbranch_execz .Lk2f_w7d1
	ds_write_b32 v16, v21 offset:33716
.Lk2f_w7d1:
	s_mov_b64 exec, s[40:41]
	v_cmp_lt_i32_e32 vcc, 2, v28
	s_and_saveexec_b64 s[40:41], vcc
	s_cbranch_execz .Lk2f_w7d2
	ds_write_b32 v16, v22 offset:33720
.Lk2f_w7d2:
	s_mov_b64 exec, s[40:41]
	v_cmp_lt_i32_e32 vcc, 3, v28
	s_and_saveexec_b64 s[40:41], vcc
	s_cbranch_execz .Lk2f_w7d3
	ds_write_b32 v16, v23 offset:33724
.Lk2f_w7d3:
	s_mov_b64 exec, s[40:41]
	v_cmp_lt_i32_e32 vcc, 0, v29
	s_and_saveexec_b64 s[40:41], vcc
	s_cbranch_execz .Lk2f_w7e0
	ds_write_b32 v17, v24 offset:33712
.Lk2f_w7e0:
	s_mov_b64 exec, s[40:41]
	v_cmp_lt_i32_e32 vcc, 1, v29
	s_and_saveexec_b64 s[40:41], vcc
	s_cbranch_execz .Lk2f_w7e1
	ds_write_b32 v17, v25 offset:33716
.Lk2f_w7e1:
	s_mov_b64 exec, s[40:41]
	v_cmp_lt_i32_e32 vcc, 2, v29
	s_and_saveexec_b64 s[40:41], vcc
	s_cbranch_execz .Lk2f_w7e2
	ds_write_b32 v17, v26 offset:33720
.Lk2f_w7e2:
	s_mov_b64 exec, s[40:41]
	v_cmp_lt_i32_e32 vcc, 3, v29
	s_and_saveexec_b64 s[40:41], vcc
	s_cbranch_execz .Lk2f_w7e3
	ds_write_b32 v17, v27 offset:33724
.Lk2f_w7e3:
	s_mov_b64 exec, s[40:41]
	v_add_u32_e32 v16, 16, v16
	v_add_u32_e32 v17, 16, v17
	v_add_u32_e32 v18, 16, v18
	s_add_i32 s5, s5, 4
	s_branch .Lk2f_w7c
.Lk2f_w7w:
	s_waitcnt lgkmcnt(0)
	v_lshlrev_b32_e32 v16, 4, v1
	v_add_u32_e32 v17, s39, v16
	v_lshlrev_b32_e32 v18, 2, v1
	s_mov_b32 s5, 0
	s_cmp_lt_u32 s5, s38
	s_cbranch_scc0 .Lk2f_exit
.Lk2f_w7x:
	v_add_u32_e32 v19, s5, v18
	v_sub_u32_e32 v19, s38, v19
	ds_read_b128 v[20:23], v16 offset:33712
	v_cmp_lt_i32_e32 vcc, 3, v19
	v_cmp_lt_i32_e64 s[42:43], 0, v19
	v_cmp_lt_i32_e64 s[44:45], 1, v19
	v_cmp_lt_i32_e64 s[46:47], 2, v19
	s_waitcnt lgkmcnt(0)
	s_andn2_b64 s[42:43], s[42:43], vcc
	s_andn2_b64 s[44:45], s[44:45], vcc
	s_andn2_b64 s[46:47], s[46:47], vcc
	s_and_saveexec_b64 s[40:41], vcc
	s_cbranch_execz .Lk2f_w7y0
	global_store_dwordx4 v17, v[20:23], s[16:17]
.Lk2f_w7y0:
	s_mov_b64 exec, s[42:43]
	s_cbranch_execz .Lk2f_w7y1
	global_store_dword v17, v20, s[16:17]
.Lk2f_w7y1:
	s_mov_b64 exec, s[44:45]
	s_cbranch_execz .Lk2f_w7y2
	global_store_dword v17, v21, s[16:17] offset:4
.Lk2f_w7y2:
	s_mov_b64 exec, s[46:47]
	s_cbranch_execz .Lk2f_w7y3
	global_store_dword v17, v22, s[16:17] offset:8
.Lk2f_w7y3:
	s_mov_b64 exec, s[40:41]
	v_add_u32_e32 v16, 0x400, v16
	v_add_u32_e32 v17, 0x400, v17
	s_addk_i32 s5, 0x100
	s_cmp_lt_u32 s5, s38
	s_cbranch_scc1 .Lk2f_w7x
	s_endpgm

	.amdhsa_kernel _Z8k_layer1PKDF16_PKiS2_PiS3_PKDv4_jS6_PKfS8_P15HIP_vector_typeIfLj2EESB_
		.amdhsa_group_segment_fixed_size 38832
		.amdhsa_private_segment_fixed_size 0
		.amdhsa_kernarg_size 88
		.amdhsa_user_sgpr_count 2
		.amdhsa_user_sgpr_dispatch_ptr 0
		.amdhsa_user_sgpr_queue_ptr 0
		.amdhsa_user_sgpr_kernarg_segment_ptr 1
		.amdhsa_user_sgpr_dispatch_id 0
		.amdhsa_user_sgpr_kernarg_preload_length 0
		.amdhsa_user_sgpr_kernarg_preload_offset 0
		.amdhsa_user_sgpr_private_segment_size 0
		.amdhsa_uses_dynamic_stack 0
		.amdhsa_enable_private_segment 0
		.amdhsa_system_sgpr_workgroup_id_x 1
		.amdhsa_system_sgpr_workgroup_id_y 0
		.amdhsa_system_sgpr_workgroup_id_z 0
		.amdhsa_system_sgpr_workgroup_info 0
		.amdhsa_system_vgpr_workitem_id 0
		.amdhsa_next_free_vgpr 64
		.amdhsa_next_free_sgpr 70
		.amdhsa_accum_offset 64
		.amdhsa_reserve_vcc 1
		.amdhsa_float_round_mode_32 0
		.amdhsa_float_round_mode_16_64 0
		.amdhsa_float_denorm_mode_32 3
		.amdhsa_float_denorm_mode_16_64 3
		.amdhsa_dx10_clamp 1
		.amdhsa_ieee_mode 1
		.amdhsa_fp16_overflow 0
		.amdhsa_tg_split 0
		.amdhsa_exception_fp_ieee_invalid_op 0
		.amdhsa_exception_fp_denorm_src 0
		.amdhsa_exception_fp_ieee_div_zero 0
		.amdhsa_exception_fp_ieee_overflow 0
		.amdhsa_exception_fp_ieee_underflow 0
		.amdhsa_exception_fp_ieee_inexact 0
		.amdhsa_exception_int_div_zero 0
	.end_amdhsa_kernel

amdhsa.kernels:
  - .agpr_count:     0
    .args:
      - .actual_access:  read_only
        .address_space:  global
        .offset:         0
        .size:           8
        .value_kind:     global_buffer
      - .actual_access:  read_only
        .address_space:  global
        .offset:         8
        .size:           8
        .value_kind:     global_buffer
      - .actual_access:  read_only
        .address_space:  global
        .offset:         16
        .size:           8
        .value_kind:     global_buffer
      - .actual_access:  read_only
        .address_space:  global
        .offset:         24
        .size:           8
        .value_kind:     global_buffer
      - .actual_access:  read_only
        .address_space:  global
        .offset:         32
        .size:           8
        .value_kind:     global_buffer
      - .actual_access:  read_only
        .address_space:  global
        .offset:         40
        .size:           8
        .value_kind:     global_buffer
      - .actual_access:  write_only
        .address_space:  global
        .offset:         48
        .size:           8
        .value_kind:     global_buffer
      - .actual_access:  write_only
        .address_space:  global
        .offset:         56
        .size:           8
        .value_kind:     global_buffer
      - .actual_access:  write_only
        .address_space:  global
        .offset:         64
        .size:           8
        .value_kind:     global_buffer
      - .actual_access:  write_only
        .address_space:  global
        .offset:         72
        .size:           8
        .value_kind:     global_buffer
      - .actual_access:  write_only
        .address_space:  global
        .offset:         80
        .size:           8
        .value_kind:     global_buffer
    .group_segment_fixed_size: 20544
    .kernarg_segment_align: 8
    .kernarg_segment_size: 88
    .language:       OpenCL C
    .language_version:
      - 2
      - 0
    .max_flat_workgroup_size: 1024
    .name:           _Z6k_partPKiPKfS2_S2_S2_S2_PiS3_PDF16_S4_S4_
    .private_segment_fixed_size: 0
    .sgpr_count:     28
    .sgpr_spill_count: 0
    .symbol:         _Z6k_partPKiPKfS2_S2_S2_S2_PiS3_PDF16_S4_S4_.kd
    .uniform_work_group_size: 1
    .uses_dynamic_stack: false
    .vgpr_count:     44
    .vgpr_spill_count: 0
    .wavefront_size: 64
  - .agpr_count:     0
    .args:
      - .actual_access:  read_only
        .address_space:  global
        .offset:         0
        .size:           8
        .value_kind:     global_buffer
      - .actual_access:  read_only
        .address_space:  global
        .offset:         8
        .size:           8
        .value_kind:     global_buffer
      - .actual_access:  read_only
        .address_space:  global
        .offset:         16
        .size:           8
        .value_kind:     global_buffer
      - .actual_access:  write_only
        .address_space:  global
        .offset:         24
        .size:           8
        .value_kind:     global_buffer
      - .address_space:  global
        .offset:         32
        .size:           8
        .value_kind:     global_buffer
      - .actual_access:  read_only
        .address_space:  global
        .offset:         40
        .size:           8
        .value_kind:     global_buffer
      - .actual_access:  read_only
        .address_space:  global
        .offset:         48
        .size:           8
        .value_kind:     global_buffer
      - .actual_access:  read_only
        .address_space:  global
        .offset:         56
        .size:           8
        .value_kind:     global_buffer
      - .actual_access:  read_only
        .address_space:  global
        .offset:         64
        .size:           8
        .value_kind:     global_buffer
      - .actual_access:  write_only
        .address_space:  global
        .offset:         72
        .size:           8
        .value_kind:     global_buffer
      - .actual_access:  write_only
        .address_space:  global
        .offset:         80
        .size:           8
        .value_kind:     global_buffer
    .group_segment_fixed_size: 38832
    .kernarg_segment_align: 8
    .kernarg_segment_size: 88
    .language:       OpenCL C
    .language_version:
      - 2
      - 0
    .max_flat_workgroup_size: 512
    .name:           _Z8k_layer1PKDF16_PKiS2_PiS3_PKDv4_jS6_PKfS8_P15HIP_vector_typeIfLj2EESB_
    .private_segment_fixed_size: 0
    .sgpr_count:     76
    .sgpr_spill_count: 0
    .symbol:         _Z8k_layer1PKDF16_PKiS2_PiS3_PKDv4_jS6_PKfS8_P15HIP_vector_typeIfLj2EESB_.kd
    .uniform_work_group_size: 1
    .uses_dynamic_stack: false
    .vgpr_count:     64
    .vgpr_spill_count: 0
    .wavefront_size: 64
  - .agpr_count:     0
    .args:
      - .actual_access:  read_only
        .address_space:  global
        .offset:         0
        .size:           8
        .value_kind:     global_buffer
      - .actual_access:  read_only
        .address_space:  global
        .offset:         8
        .size:           8
        .value_kind:     global_buffer
      - .actual_access:  read_only
        .address_space:  global
        .offset:         16
        .size:           8
        .value_kind:     global_buffer
      - .actual_access:  read_only
        .address_space:  global
        .offset:         24
        .size:           8
        .value_kind:     global_buffer
      - .actual_access:  write_only
        .address_space:  global
        .offset:         32
        .size:           8
        .value_kind:     global_buffer
    .group_segment_fixed_size: 0
    .kernarg_segment_align: 8
    .kernarg_segment_size: 40
    .language:       OpenCL C
    .language_version:
      - 2
      - 0
    .max_flat_workgroup_size: 448
    .name:           _Z8k_layer2PK15HIP_vector_typeIfLj2EES2_PKiS4_PS0_
    .private_segment_fixed_size: 0
    .sgpr_count:     21
    .sgpr_spill_count: 0
    .symbol:         _Z8k_layer2PK15HIP_vector_typeIfLj2EES2_PKiS4_PS0_.kd
    .uniform_work_group_size: 1
    .uses_dynamic_stack: false
    .vgpr_count:     25
    .vgpr_spill_count: 0
    .wavefront_size: 64
